# speedup vs baseline: 1.1034x; 1.0021x over previous
.LBB3_12:
	s_or_b64 exec, exec, s[2:3]
	v_lshlrev_b32_e32 v28, 2, v1
	s_waitcnt lgkmcnt(0)
	global_load_dword v32, v28, s[16:17]
	global_load_dword v31, v28, s[18:19]
	s_movk_i32 s38, 0xff94
	s_movk_i32 s39, 0xffee
	s_add_i32 s40, s22, -4
	v_mov_b32_e32 v131, 0x7f
	v_mov_b32_e32 v132, 0x7c
	v_min_u32_e32 v133, 27, v50
	v_min_u32_e32 v134, 3, v48
	v_or_b32_e32 v134, 24, v134
	v_lshl_or_b32 v128, v48, 6, v1
	v_mul_u32_u24_e32 v129, 0x25f, v128
	v_lshrrev_b32_e32 v129, 16, v129
	v_mad_i32_i24 v128, v129, s38, v128
	v_mul_u32_u24_e32 v130, 0xe39, v128
	v_lshrrev_b32_e32 v130, 16, v130
	v_mad_i32_i24 v128, v130, s39, v128
	v_add_u32_e32 v130, s25, v130
	v_med3_i32 v130, v130, 0, v131
	v_lshl_add_u32 v128, v128, 2, s40
	v_med3_i32 v128, v128, 0, v132
	v_min_u32_e32 v129, 15, v129
	v_lshlrev_b32_e32 v129, 14, v129
	v_lshlrev_b32_e32 v130, 7, v130
	v_or3_b32 v94, v130, v129, v128
	v_lshl_or_b32 v128, v49, 6, v1
	v_mul_u32_u24_e32 v129, 0x25f, v128
	v_lshrrev_b32_e32 v129, 16, v129
	v_mad_i32_i24 v128, v129, s38, v128
	v_mul_u32_u24_e32 v130, 0xe39, v128
	v_lshrrev_b32_e32 v130, 16, v130
	v_mad_i32_i24 v128, v130, s39, v128
	v_add_u32_e32 v130, s25, v130
	v_med3_i32 v130, v130, 0, v131
	v_lshl_add_u32 v128, v128, 2, s40
	v_med3_i32 v128, v128, 0, v132
	v_min_u32_e32 v129, 15, v129
	v_lshlrev_b32_e32 v129, 14, v129
	v_lshlrev_b32_e32 v130, 7, v130
	v_or3_b32 v96, v130, v129, v128
	v_lshl_or_b32 v128, v133, 6, v1
	v_mul_u32_u24_e32 v129, 0x25f, v128
	v_lshrrev_b32_e32 v129, 16, v129
	v_mad_i32_i24 v128, v129, s38, v128
	v_mul_u32_u24_e32 v130, 0xe39, v128
	v_lshrrev_b32_e32 v130, 16, v130
	v_mad_i32_i24 v128, v130, s39, v128
	v_add_u32_e32 v130, s25, v130
	v_med3_i32 v130, v130, 0, v131
	v_lshl_add_u32 v128, v128, 2, s40
	v_med3_i32 v128, v128, 0, v132
	v_min_u32_e32 v129, 15, v129
	v_lshlrev_b32_e32 v129, 14, v129
	v_lshlrev_b32_e32 v130, 7, v130
	v_or3_b32 v98, v130, v129, v128
	v_lshl_or_b32 v128, v134, 6, v1
	v_mul_u32_u24_e32 v129, 0x25f, v128
	v_lshrrev_b32_e32 v129, 16, v129
	v_mad_i32_i24 v128, v129, s38, v128
	v_mul_u32_u24_e32 v130, 0xe39, v128
	v_lshrrev_b32_e32 v130, 16, v130
	v_mad_i32_i24 v128, v130, s39, v128
	v_add_u32_e32 v130, s25, v130
	v_med3_i32 v130, v130, 0, v131
	v_lshl_add_u32 v128, v128, 2, s40
	v_med3_i32 v128, v128, 0, v132
	v_min_u32_e32 v129, 15, v129
	v_lshlrev_b32_e32 v129, 14, v129
	v_lshlrev_b32_e32 v130, 7, v130
	v_or3_b32 v100, v130, v129, v128
	v_cmp_eq_u32_e32 vcc, 27, v134
	v_readfirstlane_b32 s41, v100
	s_nop 1
	v_mov_b32_e32 v135, s41
	v_cndmask_b32_e32 v100, v100, v135, vcc
	v_accvgpr_write_b32 a3, 0
	v_accvgpr_write_b32 a2, 0
	v_accvgpr_write_b32 a1, 0
	v_accvgpr_write_b32 a0, 0
	v_accvgpr_write_b32 a7, 0
	v_accvgpr_write_b32 a6, 0
	v_accvgpr_write_b32 a5, 0
	v_accvgpr_write_b32 a4, 0
	v_accvgpr_write_b32 a15, 0
	v_accvgpr_write_b32 a14, 0
	v_accvgpr_write_b32 a13, 0
	v_accvgpr_write_b32 a12, 0
	v_accvgpr_write_b32 a19, 0
	v_accvgpr_write_b32 a18, 0
	v_accvgpr_write_b32 a17, 0
	v_accvgpr_write_b32 a16, 0
	v_accvgpr_write_b32 a31, 0
	v_accvgpr_write_b32 a30, 0
	v_accvgpr_write_b32 a29, 0
	v_accvgpr_write_b32 a28, 0
	v_accvgpr_write_b32 a63, 0
	v_accvgpr_write_b32 a62, 0
	v_accvgpr_write_b32 a61, 0
	v_accvgpr_write_b32 a60, 0
	v_accvgpr_write_b32 a11, 0
	v_accvgpr_write_b32 a10, 0
	v_accvgpr_write_b32 a9, 0
	v_accvgpr_write_b32 a8, 0
	v_accvgpr_write_b32 a23, 0
	v_accvgpr_write_b32 a22, 0
	v_accvgpr_write_b32 a21, 0
	v_accvgpr_write_b32 a20, 0
	v_accvgpr_write_b32 a27, 0
	v_accvgpr_write_b32 a26, 0
	v_accvgpr_write_b32 a25, 0
	v_accvgpr_write_b32 a24, 0
	v_accvgpr_write_b32 a39, 0
	v_accvgpr_write_b32 a38, 0
	v_accvgpr_write_b32 a37, 0
	v_accvgpr_write_b32 a36, 0
	v_accvgpr_write_b32 a47, 0
	v_accvgpr_write_b32 a46, 0
	v_accvgpr_write_b32 a45, 0
	v_accvgpr_write_b32 a44, 0
	v_accvgpr_write_b32 a67, 0
	v_accvgpr_write_b32 a66, 0
	v_accvgpr_write_b32 a65, 0
	v_accvgpr_write_b32 a64, 0
	v_accvgpr_write_b32 a35, 0
	v_accvgpr_write_b32 a34, 0
	v_accvgpr_write_b32 a33, 0
	v_accvgpr_write_b32 a32, 0
	v_accvgpr_write_b32 a43, 0
	v_accvgpr_write_b32 a42, 0
	v_accvgpr_write_b32 a41, 0
	v_accvgpr_write_b32 a40, 0
	v_accvgpr_write_b32 a51, 0
	v_accvgpr_write_b32 a50, 0
	v_accvgpr_write_b32 a49, 0
	v_accvgpr_write_b32 a48, 0
	v_accvgpr_write_b32 a55, 0
	v_accvgpr_write_b32 a54, 0
	v_accvgpr_write_b32 a53, 0
	v_accvgpr_write_b32 a52, 0
	v_accvgpr_write_b32 a59, 0
	v_accvgpr_write_b32 a58, 0
	v_accvgpr_write_b32 a57, 0
	v_accvgpr_write_b32 a56, 0
	v_accvgpr_write_b32 a71, 0
	v_accvgpr_write_b32 a70, 0
	v_accvgpr_write_b32 a69, 0
	v_accvgpr_write_b32 a68, 0
	s_movk_i32 s46, 0x80
	s_movk_i32 s47, 0x60
	s_movk_i32 s48, 0xffbe
	v_cmp_gt_u32_e64 s[64:65], s47, v0
	v_mov_b32_e32 v128, v47
	v_mul_u32_u24_e32 v129, 0x3e1, v128
	v_lshrrev_b32_e32 v129, 16, v129
	v_mad_i32_i24 v130, v129, s48, v128
	v_add_u32_e32 v131, s25, v129
	v_add_u32_e32 v132, s27, v130
	v_max_u32_e32 v131, v131, v132
	v_cmp_gt_u32_e64 s[50:51], s46, v131
	v_and_b32_e32 v132, 1, v130
	v_lshl_or_b32 v129, v129, 1, v132
	v_lshrrev_b32_e32 v130, 1, v130
	v_mad_u32_u24 v129, v129, 33, v130
	v_xor_b32_e32 v130, v129, v0
	v_and_b32_e32 v130, 7, v130
	v_lshlrev_b32_e32 v130, 4, v130
	v_lshl_or_b32 v140, v129, 7, v130
	v_add_u32_e32 v128, 64, v47
	v_mul_u32_u24_e32 v129, 0x3e1, v128
	v_lshrrev_b32_e32 v129, 16, v129
	v_mad_i32_i24 v130, v129, s48, v128
	v_add_u32_e32 v131, s25, v129
	v_add_u32_e32 v132, s27, v130
	v_max_u32_e32 v131, v131, v132
	v_cmp_gt_u32_e64 s[52:53], s46, v131
	v_and_b32_e32 v132, 1, v130
	v_lshl_or_b32 v129, v129, 1, v132
	v_lshrrev_b32_e32 v130, 1, v130
	v_mad_u32_u24 v129, v129, 33, v130
	v_xor_b32_e32 v130, v129, v0
	v_and_b32_e32 v130, 7, v130
	v_lshlrev_b32_e32 v130, 4, v130
	v_lshl_or_b32 v141, v129, 7, v130
	v_add_u32_e32 v128, 128, v47
	v_mul_u32_u24_e32 v129, 0x3e1, v128
	v_lshrrev_b32_e32 v129, 16, v129
	v_mad_i32_i24 v130, v129, s48, v128
	v_add_u32_e32 v131, s25, v129
	v_add_u32_e32 v132, s27, v130
	v_max_u32_e32 v131, v131, v132
	v_cmp_gt_u32_e64 s[54:55], s46, v131
	v_and_b32_e32 v132, 1, v130
	v_lshl_or_b32 v129, v129, 1, v132
	v_lshrrev_b32_e32 v130, 1, v130
	v_mad_u32_u24 v129, v129, 33, v130
	v_xor_b32_e32 v130, v129, v0
	v_and_b32_e32 v130, 7, v130
	v_lshlrev_b32_e32 v130, 4, v130
	v_lshl_or_b32 v142, v129, 7, v130
	v_add_u32_e32 v128, 192, v47
	v_mul_u32_u24_e32 v129, 0x3e1, v128
	v_lshrrev_b32_e32 v129, 16, v129
	v_mad_i32_i24 v130, v129, s48, v128
	v_add_u32_e32 v131, s25, v129
	v_add_u32_e32 v132, s27, v130
	v_max_u32_e32 v131, v131, v132
	v_cmp_gt_u32_e64 s[56:57], s46, v131
	v_and_b32_e32 v132, 1, v130
	v_lshl_or_b32 v129, v129, 1, v132
	v_lshrrev_b32_e32 v130, 1, v130
	v_mad_u32_u24 v129, v129, 33, v130
	v_xor_b32_e32 v130, v129, v0
	v_and_b32_e32 v130, 7, v130
	v_lshlrev_b32_e32 v130, 4, v130
	v_lshl_or_b32 v143, v129, 7, v130
	v_add_u32_e32 v128, 256, v47
	v_mul_u32_u24_e32 v129, 0x3e1, v128
	v_lshrrev_b32_e32 v129, 16, v129
	v_mad_i32_i24 v130, v129, s48, v128
	v_add_u32_e32 v131, s25, v129
	v_add_u32_e32 v132, s27, v130
	v_max_u32_e32 v131, v131, v132
	v_cmp_gt_u32_e64 s[58:59], s46, v131
	v_and_b32_e32 v132, 1, v130
	v_lshl_or_b32 v129, v129, 1, v132
	v_lshrrev_b32_e32 v130, 1, v130
	v_mad_u32_u24 v129, v129, 33, v130
	v_xor_b32_e32 v130, v129, v0
	v_and_b32_e32 v130, 7, v130
	v_lshlrev_b32_e32 v130, 4, v130
	v_lshl_or_b32 v144, v129, 7, v130
	v_add_u32_e32 v128, 320, v47
	v_mul_u32_u24_e32 v129, 0x3e1, v128
	v_lshrrev_b32_e32 v129, 16, v129
	v_mad_i32_i24 v130, v129, s48, v128
	v_add_u32_e32 v131, s25, v129
	v_add_u32_e32 v132, s27, v130
	v_max_u32_e32 v131, v131, v132
	v_cmp_gt_u32_e64 s[60:61], s46, v131
	v_and_b32_e32 v132, 1, v130
	v_lshl_or_b32 v129, v129, 1, v132
	v_lshrrev_b32_e32 v130, 1, v130
	v_mad_u32_u24 v129, v129, 33, v130
	v_xor_b32_e32 v130, v129, v0
	v_and_b32_e32 v130, 7, v130
	v_lshlrev_b32_e32 v130, 4, v130
	v_lshl_or_b32 v145, v129, 7, v130
	v_add_u32_e32 v128, 384, v47
	v_mul_u32_u24_e32 v129, 0x3e1, v128
	v_lshrrev_b32_e32 v129, 16, v129
	v_mad_i32_i24 v130, v129, s48, v128
	v_add_u32_e32 v131, s25, v129
	v_add_u32_e32 v132, s27, v130
	v_max_u32_e32 v131, v131, v132
	v_cmp_gt_u32_e64 s[62:63], s46, v131
	v_and_b32_e32 v132, 1, v130
	v_lshl_or_b32 v129, v129, 1, v132
	v_lshrrev_b32_e32 v130, 1, v130
	v_mad_u32_u24 v129, v129, 33, v130
	v_xor_b32_e32 v130, v129, v0
	v_and_b32_e32 v130, 7, v130
	v_lshlrev_b32_e32 v130, 4, v130
	v_lshl_or_b32 v146, v129, 7, v130
	s_waitcnt vmcnt(0)
	v_mov_b32_dpp v28, v26 row_shr:1 row_mask:0xf bank_mask:0xf bound_ctrl:1
	v_mov_b32_dpp v29, v27 row_shr:1 row_mask:0xf bank_mask:0xf bound_ctrl:1
	v_pk_add_f32 v[26:27], v[26:27], v[28:29]
	v_mov_b32_e32 v34, 0
	v_mov_b32_e32 v35, 0
	v_mov_b32_dpp v28, v26 row_shr:2 row_mask:0xf bank_mask:0xf bound_ctrl:1
	v_mov_b32_dpp v29, v27 row_shr:2 row_mask:0xf bank_mask:0xf bound_ctrl:1
	v_pk_add_f32 v[26:27], v[26:27], v[28:29]
	v_cmp_eq_u32_e32 vcc, 63, v1
	s_nop 0
	v_mov_b32_dpp v28, v26 row_shr:4 row_mask:0xf bank_mask:0xf bound_ctrl:1
	v_mov_b32_dpp v29, v27 row_shr:4 row_mask:0xf bank_mask:0xf bound_ctrl:1
	v_pk_add_f32 v[26:27], v[26:27], v[28:29]
	s_nop 1
	v_mov_b32_dpp v28, v26 row_shr:8 row_mask:0xf bank_mask:0xf bound_ctrl:1
	v_mov_b32_dpp v29, v27 row_shr:8 row_mask:0xf bank_mask:0xf bound_ctrl:1
	v_pk_add_f32 v[28:29], v[26:27], v[28:29]
	v_mov_b32_e32 v27, 0
	v_mov_b32_e32 v26, 0
	v_mov_b32_dpp v34, v28 row_bcast:15 row_mask:0xa bank_mask:0xf
	v_mov_b32_dpp v35, v29 row_bcast:15 row_mask:0xa bank_mask:0xf
	v_pk_add_f32 v[28:29], v[28:29], v[34:35]
	s_nop 1
	v_mov_b32_dpp v26, v28 row_bcast:31 row_mask:0xc bank_mask:0xf
	v_mov_b32_dpp v27, v29 row_bcast:31 row_mask:0xc bank_mask:0xf
	s_and_saveexec_b64 s[2:3], vcc
	v_lshl_add_u32 v33, v48, 3, 0
	v_add_u32_e32 v33, 0x15800, v33
	v_pk_add_f32 v[26:27], v[28:29], v[26:27]
	ds_write_b64 v33, v[26:27]
	s_or_b64 exec, exec, s[2:3]
	v_cmp_gt_u32_e32 vcc, 64, v0
	s_waitcnt lgkmcnt(0)
	s_barrier
	s_and_saveexec_b64 s[10:11], vcc
	s_cbranch_execz .LBB3_16
	s_add_i32 s2, 0, 0x15800
	v_mov_b32_e32 v26, s2
	s_add_i32 s2, 0, 0x15810
	v_mov_b32_e32 v33, s2
	ds_read_b128 v[26:29], v26
	ds_read_b128 v[34:37], v33
	s_mov_b32 s2, 0xf800000
	s_waitcnt lgkmcnt(1)
	v_add_f32_e32 v26, v26, v28
	s_waitcnt lgkmcnt(0)
	v_add_f32_e32 v28, v34, v36
	v_add_f32_e32 v26, v26, v28
	v_add_f32_e32 v27, v27, v29
	v_add_f32_e32 v28, v35, v37
	v_add_f32_e32 v27, v27, v28
	v_mul_f32_e32 v26, 0x35800000, v26
	v_mul_f32_e32 v27, 0x35800000, v27
	v_fma_f32 v27, -v26, v26, v27
	v_add_f32_e32 v27, 0x3727c5ac, v27
	v_mul_f32_e32 v28, 0x4f800000, v27
	v_cmp_gt_f32_e32 vcc, s2, v27
	s_nop 1
	v_cndmask_b32_e32 v27, v27, v28, vcc
	v_sqrt_f32_e32 v28, v27
	s_nop 0
	v_add_u32_e32 v29, -1, v28
	v_fma_f32 v33, -v29, v28, v27
	v_cmp_ge_f32_e64 s[2:3], 0, v33
	v_add_u32_e32 v33, 1, v28
	s_nop 0
	v_cndmask_b32_e64 v29, v28, v29, s[2:3]
	v_fma_f32 v28, -v33, v28, v27
	v_cmp_lt_f32_e64 s[2:3], 0, v28
	s_nop 1
	v_cndmask_b32_e64 v28, v29, v33, s[2:3]
	v_mul_f32_e32 v29, 0x37800000, v28
	v_cndmask_b32_e32 v28, v28, v29, vcc
	v_mov_b32_e32 v29, 0x260
	v_cmp_class_f32_e32 vcc, v27, v29
	s_nop 1
	v_cndmask_b32_e32 v27, v28, v27, vcc
	v_div_scale_f32 v28, s[2:3], v27, v27, 1.0
	v_rcp_f32_e32 v29, v28
	s_nop 0
	v_fma_f32 v33, -v28, v29, 1.0
	v_fmac_f32_e32 v29, v33, v29
	v_div_scale_f32 v33, vcc, 1.0, v27, 1.0
	v_mul_f32_e32 v34, v33, v29
	v_fma_f32 v35, -v28, v34, v33
	v_fmac_f32_e32 v34, v35, v29
	v_fma_f32 v28, -v28, v34, v33
	v_div_fmas_f32 v28, v28, v29, v34
	v_div_fixup_f32 v27, v28, v27, 1.0
	v_lshl_add_u32 v28, v0, 2, 0
	v_mul_f32_e32 v27, v32, v27
	v_add_u32_e32 v29, 0x15600, v28
	ds_write_b32 v29, v27
	v_fma_f32 v26, -v26, v27, v31
	v_add_u32_e32 v27, 0x15700, v28
	ds_write_b32 v27, v26
.LBB3_16:
	s_or_b64 exec, exec, s[10:11]
	v_lshlrev_b32_e32 v34, 2, v30
	s_add_i32 s2, 0, 0x15600
	s_add_i32 s3, 0, 0x15700
	v_add_u32_e32 v26, s2, v34
	v_add_u32_e32 v30, s3, v34
	s_waitcnt lgkmcnt(0)
	s_barrier
	ds_read_b128 v[26:29], v26
	ds_read_b128 v[30:33], v30
	v_or_b32_e32 v34, 16, v34
	v_add_u32_e32 v35, s2, v34
	v_add_u32_e32 v38, s3, v34
	ds_read_b128 v[34:37], v35
	ds_read_b128 v[38:41], v38
	s_load_dwordx2 s[2:3], s[0:1], 0x28
	s_waitcnt lgkmcnt(0)
	v_fma_mixlo_f16 v128, v42, v26, v30 op_sel_hi:[1,0,0]
	v_fma_mixlo_f16 v129, v43, v28, v32 op_sel_hi:[1,0,0]
	v_fma_mixlo_f16 v130, v44, v34, v38 op_sel_hi:[1,0,0]
	v_fma_mixlo_f16 v131, v45, v36, v40 op_sel_hi:[1,0,0]
	v_fma_mixhi_f16 v128, v42, v27, v31 op_sel:[1,0,0] op_sel_hi:[1,0,0]
	v_fma_mixhi_f16 v129, v43, v29, v33 op_sel:[1,0,0] op_sel_hi:[1,0,0]
	v_fma_mixhi_f16 v130, v44, v35, v39 op_sel:[1,0,0] op_sel_hi:[1,0,0]
	v_fma_mixhi_f16 v131, v45, v37, v41 op_sel:[1,0,0] op_sel_hi:[1,0,0]
	v_pk_max_f16 v128, v128, 0
	v_pk_max_f16 v129, v129, 0
	v_pk_max_f16 v130, v130, 0
	v_pk_max_f16 v131, v131, 0
	v_cndmask_b32_e64 v128, 0, v128, s[50:51]
	v_cndmask_b32_e64 v129, 0, v129, s[50:51]
	v_cndmask_b32_e64 v130, 0, v130, s[50:51]
	v_cndmask_b32_e64 v131, 0, v131, s[50:51]
	ds_write_b128 v140, v[128:131]
	v_fma_mixlo_f16 v132, v22, v26, v30 op_sel_hi:[1,0,0]
	v_fma_mixlo_f16 v133, v23, v28, v32 op_sel_hi:[1,0,0]
	v_fma_mixlo_f16 v134, v24, v34, v38 op_sel_hi:[1,0,0]
	v_fma_mixlo_f16 v135, v25, v36, v40 op_sel_hi:[1,0,0]
	v_fma_mixhi_f16 v132, v22, v27, v31 op_sel:[1,0,0] op_sel_hi:[1,0,0]
	v_fma_mixhi_f16 v133, v23, v29, v33 op_sel:[1,0,0] op_sel_hi:[1,0,0]
	v_fma_mixhi_f16 v134, v24, v35, v39 op_sel:[1,0,0] op_sel_hi:[1,0,0]
	v_fma_mixhi_f16 v135, v25, v37, v41 op_sel:[1,0,0] op_sel_hi:[1,0,0]
	v_pk_max_f16 v132, v132, 0
	v_pk_max_f16 v133, v133, 0
	v_pk_max_f16 v134, v134, 0
	v_pk_max_f16 v135, v135, 0
	v_cndmask_b32_e64 v132, 0, v132, s[52:53]
	v_cndmask_b32_e64 v133, 0, v133, s[52:53]
	v_cndmask_b32_e64 v134, 0, v134, s[52:53]
	v_cndmask_b32_e64 v135, 0, v135, s[52:53]
	ds_write_b128 v141, v[132:135]
	v_fma_mixlo_f16 v128, v18, v26, v30 op_sel_hi:[1,0,0]
	v_fma_mixlo_f16 v129, v19, v28, v32 op_sel_hi:[1,0,0]
	v_fma_mixlo_f16 v130, v20, v34, v38 op_sel_hi:[1,0,0]
	v_fma_mixlo_f16 v131, v21, v36, v40 op_sel_hi:[1,0,0]
	v_fma_mixhi_f16 v128, v18, v27, v31 op_sel:[1,0,0] op_sel_hi:[1,0,0]
	v_fma_mixhi_f16 v129, v19, v29, v33 op_sel:[1,0,0] op_sel_hi:[1,0,0]
	v_fma_mixhi_f16 v130, v20, v35, v39 op_sel:[1,0,0] op_sel_hi:[1,0,0]
	v_fma_mixhi_f16 v131, v21, v37, v41 op_sel:[1,0,0] op_sel_hi:[1,0,0]
	v_pk_max_f16 v128, v128, 0
	v_pk_max_f16 v129, v129, 0
	v_pk_max_f16 v130, v130, 0
	v_pk_max_f16 v131, v131, 0
	v_cndmask_b32_e64 v128, 0, v128, s[54:55]
	v_cndmask_b32_e64 v129, 0, v129, s[54:55]
	v_cndmask_b32_e64 v130, 0, v130, s[54:55]
	v_cndmask_b32_e64 v131, 0, v131, s[54:55]
	ds_write_b128 v142, v[128:131]
	v_fma_mixlo_f16 v132, v14, v26, v30 op_sel_hi:[1,0,0]
	v_fma_mixlo_f16 v133, v15, v28, v32 op_sel_hi:[1,0,0]
	v_fma_mixlo_f16 v134, v16, v34, v38 op_sel_hi:[1,0,0]
	v_fma_mixlo_f16 v135, v17, v36, v40 op_sel_hi:[1,0,0]
	v_fma_mixhi_f16 v132, v14, v27, v31 op_sel:[1,0,0] op_sel_hi:[1,0,0]
	v_fma_mixhi_f16 v133, v15, v29, v33 op_sel:[1,0,0] op_sel_hi:[1,0,0]
	v_fma_mixhi_f16 v134, v16, v35, v39 op_sel:[1,0,0] op_sel_hi:[1,0,0]
	v_fma_mixhi_f16 v135, v17, v37, v41 op_sel:[1,0,0] op_sel_hi:[1,0,0]
	v_pk_max_f16 v132, v132, 0
	v_pk_max_f16 v133, v133, 0
	v_pk_max_f16 v134, v134, 0
	v_pk_max_f16 v135, v135, 0
	v_cndmask_b32_e64 v132, 0, v132, s[56:57]
	v_cndmask_b32_e64 v133, 0, v133, s[56:57]
	v_cndmask_b32_e64 v134, 0, v134, s[56:57]
	v_cndmask_b32_e64 v135, 0, v135, s[56:57]
	ds_write_b128 v143, v[132:135]
	v_fma_mixlo_f16 v128, v10, v26, v30 op_sel_hi:[1,0,0]
	v_fma_mixlo_f16 v129, v11, v28, v32 op_sel_hi:[1,0,0]
	v_fma_mixlo_f16 v130, v12, v34, v38 op_sel_hi:[1,0,0]
	v_fma_mixlo_f16 v131, v13, v36, v40 op_sel_hi:[1,0,0]
	v_fma_mixhi_f16 v128, v10, v27, v31 op_sel:[1,0,0] op_sel_hi:[1,0,0]
	v_fma_mixhi_f16 v129, v11, v29, v33 op_sel:[1,0,0] op_sel_hi:[1,0,0]
	v_fma_mixhi_f16 v130, v12, v35, v39 op_sel:[1,0,0] op_sel_hi:[1,0,0]
	v_fma_mixhi_f16 v131, v13, v37, v41 op_sel:[1,0,0] op_sel_hi:[1,0,0]
	v_pk_max_f16 v128, v128, 0
	v_pk_max_f16 v129, v129, 0
	v_pk_max_f16 v130, v130, 0
	v_pk_max_f16 v131, v131, 0
	v_cndmask_b32_e64 v128, 0, v128, s[58:59]
	v_cndmask_b32_e64 v129, 0, v129, s[58:59]
	v_cndmask_b32_e64 v130, 0, v130, s[58:59]
	v_cndmask_b32_e64 v131, 0, v131, s[58:59]
	ds_write_b128 v144, v[128:131]
	v_fma_mixlo_f16 v132, v6, v26, v30 op_sel_hi:[1,0,0]
	v_fma_mixlo_f16 v133, v7, v28, v32 op_sel_hi:[1,0,0]
	v_fma_mixlo_f16 v134, v8, v34, v38 op_sel_hi:[1,0,0]
	v_fma_mixlo_f16 v135, v9, v36, v40 op_sel_hi:[1,0,0]
	v_fma_mixhi_f16 v132, v6, v27, v31 op_sel:[1,0,0] op_sel_hi:[1,0,0]
	v_fma_mixhi_f16 v133, v7, v29, v33 op_sel:[1,0,0] op_sel_hi:[1,0,0]
	v_fma_mixhi_f16 v134, v8, v35, v39 op_sel:[1,0,0] op_sel_hi:[1,0,0]
	v_fma_mixhi_f16 v135, v9, v37, v41 op_sel:[1,0,0] op_sel_hi:[1,0,0]
	v_pk_max_f16 v132, v132, 0
	v_pk_max_f16 v133, v133, 0
	v_pk_max_f16 v134, v134, 0
	v_pk_max_f16 v135, v135, 0
	v_cndmask_b32_e64 v132, 0, v132, s[60:61]
	v_cndmask_b32_e64 v133, 0, v133, s[60:61]
	v_cndmask_b32_e64 v134, 0, v134, s[60:61]
	v_cndmask_b32_e64 v135, 0, v135, s[60:61]
	ds_write_b128 v145, v[132:135]
	s_mov_b64 exec, s[64:65]
	v_fma_mixlo_f16 v128, v2, v26, v30 op_sel_hi:[1,0,0]
	v_fma_mixlo_f16 v129, v3, v28, v32 op_sel_hi:[1,0,0]
	v_fma_mixlo_f16 v130, v4, v34, v38 op_sel_hi:[1,0,0]
	v_fma_mixlo_f16 v131, v5, v36, v40 op_sel_hi:[1,0,0]
	v_fma_mixhi_f16 v128, v2, v27, v31 op_sel:[1,0,0] op_sel_hi:[1,0,0]
	v_fma_mixhi_f16 v129, v3, v29, v33 op_sel:[1,0,0] op_sel_hi:[1,0,0]
	v_fma_mixhi_f16 v130, v4, v35, v39 op_sel:[1,0,0] op_sel_hi:[1,0,0]
	v_fma_mixhi_f16 v131, v5, v37, v41 op_sel:[1,0,0] op_sel_hi:[1,0,0]
	v_pk_max_f16 v128, v128, 0
	v_pk_max_f16 v129, v129, 0
	v_pk_max_f16 v130, v130, 0
	v_pk_max_f16 v131, v131, 0
	v_cndmask_b32_e64 v128, 0, v128, s[62:63]
	v_cndmask_b32_e64 v129, 0, v129, s[62:63]
	v_cndmask_b32_e64 v130, 0, v130, s[62:63]
	v_cndmask_b32_e64 v131, 0, v131, s[62:63]
	ds_write_b128 v146, v[128:131]
	s_mov_b64 exec, -1
	s_load_dwordx2 s[12:13], s[0:1], 0x30
	v_min_u32_e32 v47, 27, v50
	v_min_u32_e32 v2, 3, v48
	v_or_b32_e32 v56, 24, v2
	v_lshrrev_b32_e32 v122, 4, v1
	v_and_b32_e32 v93, 15, v0
	v_lshrrev_b32_e32 v120, 8, v0
	s_lshl_b32 s18, s24, 18
	v_and_b32_e32 v121, 3, v48
	v_lshl_or_b32 v123, v120, 4, v93
	s_movk_i32 s0, 0x42
	s_cmp_lg_u32 0, -1
	v_mad_u32_u24 v1, v121, s0, v123
	s_cselect_b32 s0, 0, 0
	v_lshlrev_b32_e32 v2, 7, v1
	v_bitop3_b32 v3, v1, v122, 7 bitop3:0x6c
	v_add_u32_e32 v1, 33, v1
	s_add_i32 s1, s0, 0xc600
	v_lshl_or_b32 v126, v3, 4, v2
	v_lshlrev_b32_e32 v2, 7, v1
	v_bitop3_b32 v1, v1, v122, 7 bitop3:0x6c
	v_add_u32_e32 v124, s1, v46
	s_add_i32 s1, s0, 0xca00
	v_lshl_or_b32 v127, v1, 4, v2
	v_add_u32_e32 v1, s1, v46
	s_add_i32 s1, s0, 0xce00
	s_waitcnt vmcnt(0)
	s_waitcnt lgkmcnt(0)
	s_barrier
	ds_read_b128 v[42:45], v124
	ds_read_b128 v[38:41], v1
	v_add_u32_e32 v1, s1, v46
	s_add_i32 s1, s0, 0xd200
	ds_read_b128 v[34:37], v1
	v_add_u32_e32 v1, s1, v46
	s_add_i32 s1, s0, 0xd600
	ds_read_b128 v[30:33], v1
	v_add_u32_e32 v1, s1, v46
	s_add_i32 s1, s0, 0xda00
	ds_read_b128 v[26:29], v1
	v_add_u32_e32 v1, s1, v46
	s_add_i32 s1, s0, 0xde00
	ds_read_b128 v[22:25], v1
	v_add_u32_e32 v1, s1, v46
	s_add_i32 s1, s0, 0xe200
	ds_read_b128 v[10:13], v1
	v_add_u32_e32 v1, s1, v46
	s_add_i32 s1, s0, 0xe600
	ds_read_b128 v[6:9], v1
	v_add_u32_e32 v1, s1, v46
	ds_read_b128 v[2:5], v1
	v_add_u32_e32 v1, s0, v126
	ds_read_b128 v[14:17], v1
	v_add_u32_e32 v1, s0, v127
	s_add_i32 s0, s0, 0xea00
	v_add_u32_e32 v125, s0, v46
	s_lshl_b32 s0, s24, 20
	s_add_u32 s10, s2, s0
	v_mov_b32_e32 v95, 0
	v_lshlrev_b32_e32 v0, 4, v0
	ds_read_b128 v[18:21], v1
	s_addc_u32 s11, s3, 0
	v_lshlrev_b32_e32 v91, 10, v47
	v_and_b32_e32 v0, 0x1c00, v0
	v_mov_b32_e32 v1, v95
	v_mov_b32_e32 v47, 0x28800
	s_add_u32 s0, s10, 0x400000
	v_mad_u64_u32 v[54:55], s[2:3], s24, v47, v[0:1]
	s_addc_u32 s1, s11, 0
	v_lshlrev_b32_e32 v48, 2, v94
	v_mov_b32_e32 v49, v95
	v_lshlrev_b32_e32 v50, 2, v96
	v_mov_b32_e32 v51, v95
	v_lshlrev_b32_e32 v52, 2, v98
	v_mov_b32_e32 v53, v95
	v_or_b32_e32 v54, v54, v46
	v_lshlrev_b32_e32 v46, 2, v100
	v_mov_b32_e32 v47, v95
	s_waitcnt lgkmcnt(0)
	v_lshl_add_u64 v[0:1], s[0:1], 0, v[48:49]
	v_lshl_add_u64 v[106:107], s[0:1], 0, v[50:51]
	v_lshl_add_u64 v[110:111], s[0:1], 0, v[52:53]
	v_lshl_add_u64 v[112:113], s[10:11], 0, v[46:47]
	v_lshl_add_u64 v[114:115], s[0:1], 0, v[46:47]
	v_lshl_add_u64 v[46:47], s[20:21], 0, v[54:55]
	s_mov_b64 s[0:1], 0xd000
	v_lshl_add_u64 v[116:117], v[46:47], 0, s[0:1]
	s_movk_i32 s0, 0xc000
	s_movk_i32 s2, 0xe000
	s_mov_b32 s19, 0
	v_lshl_add_u64 v[102:103], s[10:11], 0, v[48:49]
	v_mov_b32_e32 v97, v95
	v_mov_b32_e32 v99, v95
	v_mov_b32_e32 v101, v95
	v_lshlrev_b32_e32 v119, 10, v56
	v_lshl_add_u64 v[104:105], s[10:11], 0, v[50:51]
	v_lshl_add_u64 v[108:109], s[10:11], 0, v[52:53]
	s_mov_b32 s20, 1
	s_mov_b32 s1, -1
	s_mov_b32 s3, -1
	s_add_i32 s17, 0, 0x16000
	s_add_i32 s16, 0, 0x1d000
	s_mov_b64 s[6:7], 0x4800
	v_readfirstlane_b32 s32, v118
	v_readfirstlane_b32 s33, v90
	v_readfirstlane_b32 s34, v92
	s_nop 3
	s_add_i32 s32, s32, 0xc600
	s_add_i32 s33, s33, 0xc600
	s_add_i32 s34, s34, 0xc600

	.amdhsa_kernel _Z7kfinal3PKDF16_PKfS2_S2_PK15HIP_vector_typeIjLj4EES2_Pf
		.amdhsa_group_segment_fixed_size 0
		.amdhsa_private_segment_fixed_size 0
		.amdhsa_kernarg_size 56
		.amdhsa_user_sgpr_count 2
		.amdhsa_user_sgpr_dispatch_ptr 0
		.amdhsa_user_sgpr_queue_ptr 0
		.amdhsa_user_sgpr_kernarg_segment_ptr 1
		.amdhsa_user_sgpr_dispatch_id 0
		.amdhsa_user_sgpr_kernarg_preload_length 0
		.amdhsa_user_sgpr_kernarg_preload_offset 0
		.amdhsa_user_sgpr_private_segment_size 0
		.amdhsa_uses_dynamic_stack 0
		.amdhsa_enable_private_segment 0
		.amdhsa_system_sgpr_workgroup_id_x 1
		.amdhsa_system_sgpr_workgroup_id_y 0
		.amdhsa_system_sgpr_workgroup_id_z 0
		.amdhsa_system_sgpr_workgroup_info 0
		.amdhsa_system_vgpr_workitem_id 0
		.amdhsa_next_free_vgpr 221
		.amdhsa_next_free_sgpr 66
		.amdhsa_accum_offset 148
		.amdhsa_reserve_vcc 1
		.amdhsa_float_round_mode_32 0
		.amdhsa_float_round_mode_16_64 0
		.amdhsa_float_denorm_mode_32 3
		.amdhsa_float_denorm_mode_16_64 3
		.amdhsa_dx10_clamp 1
		.amdhsa_ieee_mode 1
		.amdhsa_fp16_overflow 0
		.amdhsa_tg_split 0
		.amdhsa_exception_fp_ieee_invalid_op 0
		.amdhsa_exception_fp_denorm_src 0
		.amdhsa_exception_fp_ieee_div_zero 0
		.amdhsa_exception_fp_ieee_overflow 0
		.amdhsa_exception_fp_ieee_underflow 0
		.amdhsa_exception_fp_ieee_inexact 0
		.amdhsa_exception_int_div_zero 0
	.end_amdhsa_kernel

amdhsa.kernels:
  - .agpr_count:     0
    .args:
      - .actual_access:  read_only
        .address_space:  global
        .offset:         0
        .size:           8
        .value_kind:     global_buffer
      - .actual_access:  read_only
        .address_space:  global
        .offset:         8
        .size:           8
        .value_kind:     global_buffer
      - .actual_access:  read_only
        .address_space:  global
        .offset:         16
        .size:           8
        .value_kind:     global_buffer
      - .actual_access:  read_only
        .address_space:  global
        .offset:         24
        .size:           8
        .value_kind:     global_buffer
      - .actual_access:  read_only
        .address_space:  global
        .offset:         32
        .size:           8
        .value_kind:     global_buffer
      - .actual_access:  read_only
        .address_space:  global
        .offset:         40
        .size:           8
        .value_kind:     global_buffer
      - .actual_access:  write_only
        .address_space:  global
        .offset:         48
        .size:           8
        .value_kind:     global_buffer
      - .actual_access:  write_only
        .address_space:  global
        .offset:         56
        .size:           8
        .value_kind:     global_buffer
      - .actual_access:  write_only
        .address_space:  global
        .offset:         64
        .size:           8
        .value_kind:     global_buffer
      - .actual_access:  write_only
        .address_space:  global
        .offset:         72
        .size:           8
        .value_kind:     global_buffer
    .group_segment_fixed_size: 12000
    .kernarg_segment_align: 8
    .kernarg_segment_size: 80
    .language:       OpenCL C
    .language_version:
      - 2
      - 0
    .max_flat_workgroup_size: 256
    .name:           _Z2k0PKfS0_S0_S0_S0_S0_PDF16_PfS1_S1_
    .private_segment_fixed_size: 0
    .sgpr_count:     24
    .sgpr_spill_count: 0
    .symbol:         _Z2k0PKfS0_S0_S0_S0_S0_PDF16_PfS1_S1_.kd
    .uniform_work_group_size: 1
    .uses_dynamic_stack: false
    .vgpr_count:     150
    .vgpr_spill_count: 0
    .wavefront_size: 64
  - .agpr_count:     16
    .args:
      - .actual_access:  read_only
        .address_space:  global
        .offset:         0
        .size:           8
        .value_kind:     global_buffer
      - .actual_access:  read_only
        .address_space:  global
        .offset:         8
        .size:           8
        .value_kind:     global_buffer
      - .actual_access:  read_only
        .address_space:  global
        .offset:         16
        .size:           8
        .value_kind:     global_buffer
      - .actual_access:  read_only
        .address_space:  global
        .offset:         24
        .size:           8
        .value_kind:     global_buffer
      - .actual_access:  read_only
        .address_space:  global
        .offset:         32
        .size:           8
        .value_kind:     global_buffer
      - .actual_access:  write_only
        .address_space:  global
        .offset:         40
        .size:           8
        .value_kind:     global_buffer
      - .actual_access:  write_only
        .address_space:  global
        .offset:         48
        .size:           8
        .value_kind:     global_buffer
    .group_segment_fixed_size: 14112
    .kernarg_segment_align: 8
    .kernarg_segment_size: 56
    .language:       OpenCL C
    .language_version:
      - 2
      - 0
    .max_flat_workgroup_size: 256
    .name:           _Z4khidPKDF16_PKfS2_S2_S0_PDF16_Pf
    .private_segment_fixed_size: 0
    .sgpr_count:     24
    .sgpr_spill_count: 0
    .symbol:         _Z4khidPKDF16_PKfS2_S2_S0_PDF16_Pf.kd
    .uniform_work_group_size: 1
    .uses_dynamic_stack: false
    .vgpr_count:     148
    .vgpr_spill_count: 0
    .wavefront_size: 64
  - .agpr_count:     144
    .args:
      - .actual_access:  read_only
        .address_space:  global
        .offset:         0
        .size:           8
        .value_kind:     global_buffer
      - .actual_access:  read_only
        .address_space:  global
        .offset:         8
        .size:           8
        .value_kind:     global_buffer
      - .actual_access:  read_only
        .address_space:  global
        .offset:         16
        .size:           8
        .value_kind:     global_buffer
      - .actual_access:  read_only
        .address_space:  global
        .offset:         24
        .size:           8
        .value_kind:     global_buffer
      - .address_space:  global
        .offset:         32
        .size:           8
        .value_kind:     global_buffer
      - .address_space:  global
        .offset:         40
        .size:           8
        .value_kind:     global_buffer
      - .address_space:  global
        .offset:         48
        .size:           8
        .value_kind:     global_buffer
    .group_segment_fixed_size: 0
    .kernarg_segment_align: 8
    .kernarg_segment_size: 56
    .language:       OpenCL C
    .language_version:
      - 2
      - 0
    .max_flat_workgroup_size: 256
    .name:           _Z6kfinalPKDF16_PKfS2_S2_PK15HIP_vector_typeIjLj4EES2_Pf
    .private_segment_fixed_size: 0
    .sgpr_count:     41
    .sgpr_spill_count: 0
    .symbol:         _Z6kfinalPKDF16_PKfS2_S2_PK15HIP_vector_typeIjLj4EES2_Pf.kd
    .uniform_work_group_size: 1
    .uses_dynamic_stack: false
    .vgpr_count:     400
    .vgpr_spill_count: 0
    .wavefront_size: 64
  - .agpr_count:     73
    .args:
      - .actual_access:  read_only
        .address_space:  global
        .offset:         0
        .size:           8
        .value_kind:     global_buffer
      - .actual_access:  read_only
        .address_space:  global
        .offset:         8
        .size:           8
        .value_kind:     global_buffer
      - .actual_access:  read_only
        .address_space:  global
        .offset:         16
        .size:           8
        .value_kind:     global_buffer
      - .actual_access:  read_only
        .address_space:  global
        .offset:         24
        .size:           8
        .value_kind:     global_buffer
      - .address_space:  global
        .offset:         32
        .size:           8
        .value_kind:     global_buffer
      - .address_space:  global
        .offset:         40
        .size:           8
        .value_kind:     global_buffer
      - .address_space:  global
        .offset:         48
        .size:           8
        .value_kind:     global_buffer
    .group_segment_fixed_size: 0
    .kernarg_segment_align: 8
    .kernarg_segment_size: 56
    .language:       OpenCL C
    .language_version:
      - 2
      - 0
    .max_flat_workgroup_size: 512
    .name:           _Z7kfinal3PKDF16_PKfS2_S2_PK15HIP_vector_typeIjLj4EES2_Pf
    .private_segment_fixed_size: 0
    .sgpr_count:     72
    .sgpr_spill_count: 0
    .symbol:         _Z7kfinal3PKDF16_PKfS2_S2_PK15HIP_vector_typeIjLj4EES2_Pf.kd
    .uniform_work_group_size: 1
    .uses_dynamic_stack: false
    .vgpr_count:     221
    .vgpr_spill_count: 0
    .wavefront_size: 64
